# attention unit prologues (P19, P12, P3): instructions independent of the Q loads (LDS-DMA address math and the first tile DMAs) hoisted above the wait for Q, temporaries renamed to free VGPRs, vmcnt c
# speedup vs baseline: 1.0019x; 1.0019x over previous
; template <int MODE, int DQK, int DV>
; __device__ __forceinline__ void attn_pass(LAS unsigned char* lds, const Tens& T, size_t rowbase, int q0, f32x16 (&o)[DV / 32], float& l_out, const int wave, QPre* qp = nullptr) {
;     ...
;         const bf16* qp = T.Q + (rowbase + tq) * (size_t)T.ldq + 8 * h;
; #pragma unroll
;         for (int s = 0; s < NSTEP; ++s) qf[s] = *(const bf16x8*)(qp + 16 * s);
;     }
;     {
;         f32x4 c0 = {1.f, 1.f, 1.f, 1.f}, c1 = c0, s0 = {0.f, 0.f, 0.f, 0.f}, s1 = s0;
;         if (MODE == AM_MLA) {
;             c0 = *(const f32x4*)(T.rcos + tq * 16 + 8 * h); c1 = *(const f32x4*)(T.rcos + tq * 16 + 8 * h + 4);
;             s0 = *(const f32x4*)(T.rsin + tq * 16 + 8 * h); s1 = *(const f32x4*)(T.rsin + tq * 16 + 8 * h + 4);
;         }
; #pragma unroll
;         for (int s = 0; s < NSTEP; ++s) {
;             if (MODE == AM_MLA && s == NSTEP - 1) continue;
;             bf16x8 a = qf[s];
;             if (MODE == AM_MLA && s == NSTEP - 2) {
;                 bf16x8 b2 = qf[NSTEP - 1];
; #pragma unroll
;                 for (int j = 0; j < 8; ++j) {
;                     const float x1 = __uint_as_float(((unsigned)(unsigned short)a[j]) << 16), x2 = __uint_as_float(((unsigned)(unsigned short)b2[j]) << 16);
;                     const float cs = j < 4 ? c0[j & 3] : c1[j & 3], sn = j < 4 ? s0[j & 3] : s1[j & 3];
;                     a[j] = (short)f2bf((x1 * cs - x2 * sn) * T.scale2); b2[j] = (short)f2bf((x2 * cs + x1 * sn) * T.scale2);
;                 }
;                 qf[NSTEP - 1] = b2;
;             } else {
; #pragma unroll
;                 for (int j = 0; j < 8; ++j) a[j] = (short)f2bf(__uint_as_float(((unsigned)(unsigned short)a[j]) << 16) * T.scale2);
;             }
;             qf[s] = a;
;         }
;     }
;     ...
;     const unsigned lds0 = (unsigned)(uintptr_t)lds;
;     ...
;     const unsigned kvo = (unsigned)(dk_key * T.ldk + dk_col) * 2u, rvo = (unsigned)(dr_key * T.ldk2 + dr_col) * 2u;
;     unsigned vvo[DV / 64];
; #pragma unroll
;     for (int n = 0; n < DV / 64; ++n) vvo[n] = (unsigned)(dv_key[n] * T.ldv + dv_col[n]) * 2u;
;     const unsigned cvo = (unsigned)lane * 32u, mvo = (unsigned)(wave * 64 + lane) * 4u;
;     const char* const ubK = (const char*)(T.K + rowbase * (size_t)T.ldk);
;     const char* const ubK2 = (MODE == AM_MLA) ? (const char*)(T.K2 + rowbase * (size_t)T.ldk2) : nullptr;
.LBB0_632:
	v_add_u32_e32 v0, 0, v0
	s_waitcnt lgkmcnt(0)
	s_barrier
	ds_read_b32 v0, v0
	s_waitcnt lgkmcnt(0)
	s_barrier
	v_readfirstlane_b32 s1, v0
	s_cmp_lt_i32 s1, 0
	s_cbranch_scc1 .LBB0_711
	s_lshr_b32 s2, s1, 5
	s_and_b32 s2, s2, 6
	s_bfe_u32 s3, s1, 0x10004
	s_lshr_b32 s44, s1, 8
	s_or_b32 s4, s2, s3
	s_and_b32 s2, s1, 32
	s_and_b32 s1, s1, 15
	s_cmp_eq_u32 s2, 0
	s_cselect_b32 s2, 31, 15
	s_xor_b32 s1, s2, s1
	s_lshl_b32 s2, s4, 7
	v_readlane_b32 s3, v254, 30
	s_add_u32 s10, s3, s2
	v_readlane_b32 s3, v254, 31
	s_addc_u32 s11, s3, 0
	v_readlane_b32 s3, v254, 33
	s_add_u32 s5, s3, s2
	v_readlane_b32 s3, v254, 35
	s_addc_u32 s6, s3, 0
	v_readlane_b32 s3, v254, 37
	s_add_u32 s7, s3, s2
	v_readlane_b32 s2, v254, 39
	s_addc_u32 s8, s2, 0
	s_lshl_b32 s9, s4, 2
	v_readlane_b32 s2, v254, 41
	s_add_u32 s2, s2, s9
	v_readlane_b32 s3, v254, 43
	s_addc_u32 s3, s3, 0
	s_lshl_b32 s12, s44, 5
	v_readlane_b32 s13, v254, 45
	s_add_u32 s12, s13, s12
	v_readlane_b32 s13, v254, 47
	s_addc_u32 s13, s13, 0
	v_mov_b32_e32 v0, s9
	s_lshl_b32 s83, s1, 8
	v_readlane_b32 s9, v254, 53
	s_add_i32 s82, s83, s9
	global_load_dword v3, v0, s[12:13] sc1
	v_mbcnt_lo_u32_b32 v46, -1, 0
	v_mbcnt_hi_u32_b32 v46, -1, v46
	s_lshl_b64 s[66:67], s[44:45], 13
	v_and_b32_e32 v0, 31, v46
	v_or_b32_e32 v82, s82, v0
	v_lshl_add_u64 v[36:37], s[66:67], 0, v[82:83]
	v_mov_b64_e32 v[4:5], s[10:11]
	s_movk_i32 s9, 0x1c00
	v_bfe_u32 v1, v46, 5, 1
	v_mad_u64_u32 v[4:5], s[10:11], v36, s9, v[4:5]
	v_mad_u32_u24 v5, v37, s9, v5
	v_lshlrev_b32_e32 v82, 4, v1
	v_lshl_add_u64 v[12:13], v[4:5], 0, v[82:83]
	global_load_dwordx4 v[4:7], v[12:13], off
	global_load_dwordx4 v[8:11], v[12:13], off offset:32
	global_load_dwordx4 v[24:27], v[12:13], off offset:64
	global_load_dwordx4 v[32:35], v[12:13], off offset:96
	v_lshlrev_b64 v[36:37], 5, v[36:37]
	v_lshl_add_u64 v[36:37], s[2:3], 0, v[36:37]
	global_load_dword v36, v[36:37], off
	s_add_i32 s9, s83, 0x100
	s_lshr_b32 s84, s9, 6
	v_readlane_b32 s9, v254, 49
	s_lshl_b64 s[10:11], s[44:45], 18
	v_and_b32_e32 v2, 63, v46
	v_lshlrev_b32_e32 v99, 5, v2
	v_bfe_u32 v122, v46, 3, 3
	v_or_b32_e32 v123, s9, v122
	v_lshrrev_b32_e32 v124, 4, v46
	v_lshrrev_b32_e32 v125, 2, v46
	v_lshrrev_b32_e32 v126, 1, v123
	v_xor_b32_e32 v127, v125, v124
	v_xor_b32_e32 v128, v126, v46
	v_lshlrev_b32_e32 v129, 5, v127
	v_lshlrev_b32_e32 v130, 3, v46
	s_movk_i32 s9, 0xe00
	v_lshlrev_b32_e32 v131, 3, v128
	v_and_b32_e32 v132, 32, v129
	v_and_b32_e32 v133, 24, v130
	v_mul_lo_u32 v134, v123, s9
	v_and_or_b32 v135, v131, 56, v134
	v_or3_b32 v136, v133, v132, v134
	v_bfe_u32 v137, v46, 2, 2
	v_lshlrev_b32_e32 v94, 1, v136
	v_lshlrev_b32_e32 v138, 2, v46
	v_and_or_b32 v139, v122, 4, v137
	v_and_b32_e32 v140, 16, v46
	s_add_u32 s9, s2, s10
	v_and_or_b32 v141, v138, 12, v140
	s_addc_u32 s10, s3, s11
	s_mul_i32 s3, s44, 0x3800000
	v_lshlrev_b32_e32 v142, 7, v139
	v_lshlrev_b32_e32 v143, 1, v141
	s_mul_hi_u32 s2, s44, 0x3800000
	s_add_u32 s7, s7, s3
	v_add3_u32 v144, 0, v142, v143
	v_and_b32_e32 v145, 64, v130
	s_movk_i32 s11, 0x6000
	v_lshrrev_b32_e32 v146, 1, v46
	s_addc_u32 s8, s8, s2
	v_add3_u32 v100, v144, v145, s11
	v_bitop3_b32 v147, v130, 64, v130 bitop3:0xc
	v_bfe_u32 v148, v46, 1, 3
	v_lshl_add_u32 v149, v0, 7, 0
	v_bitop3_b32 v150, v1, v146, 7 bitop3:0x78
	v_add3_u32 v101, v144, v147, s11
	s_add_u32 s11, s5, s3
	v_lshl_add_u32 v95, v150, 4, v149
	v_bitop3_b32 v151, v1, v148, 2 bitop3:0x36
	s_addc_u32 s6, s6, s2
	s_add_i32 s44, s84, -1
	v_lshl_add_u32 v96, v151, 4, v149
	v_bitop3_b32 v152, v1, v148, 4 bitop3:0x36
	s_mul_i32 s12, s44, 0x70000
	v_lshl_add_u32 v97, v152, 4, v149
	v_bitop3_b32 v153, v1, v148, 6 bitop3:0x36
	s_mul_hi_u32 s5, s44, 0x70000
	s_add_u32 s2, s11, s12
	v_lshl_add_u32 v98, v153, 4, v149
	s_addc_u32 s3, s6, s5
	v_lshlrev_b32_e32 v102, 1, v135
	s_mov_b32 m0, s80
	s_nop 0
	global_load_lds_dwordx4 v102, s[2:3]
	s_add_u32 s2, s7, s12
	s_addc_u32 s3, s8, s5
	v_readlane_b32 s12, v254, 26
	s_mov_b32 m0, s81
	s_nop 0
	global_load_lds_dwordx4 v94, s[2:3]
	v_readlane_b32 s13, v254, 27
	s_waitcnt vmcnt(2)
	v_and_b32_e32 v13, 0xffff0000, v4
	v_lshlrev_b32_e32 v12, 16, v4
	v_and_b32_e32 v15, 0xffff0000, v5
	v_lshlrev_b32_e32 v14, 16, v5
	v_and_b32_e32 v5, 0xffff0000, v6
	v_lshlrev_b32_e32 v4, 16, v6
	v_and_b32_e32 v17, 0xffff0000, v7
	v_lshlrev_b32_e32 v16, 16, v7
	v_and_b32_e32 v7, 0xffff0000, v8
	v_lshlrev_b32_e32 v6, 16, v8
	v_and_b32_e32 v19, 0xffff0000, v9
	v_lshlrev_b32_e32 v18, 16, v9
	v_and_b32_e32 v9, 0xffff0000, v10
	v_lshlrev_b32_e32 v8, 16, v10
	v_and_b32_e32 v21, 0xffff0000, v11
	v_lshlrev_b32_e32 v20, 16, v11
	v_and_b32_e32 v11, 0xffff0000, v24
	v_lshlrev_b32_e32 v10, 16, v24
	v_pk_mul_f32 v[12:13], v[12:13], s[48:49] op_sel_hi:[1,0]
	v_pk_mul_f32 v[14:15], v[14:15], s[48:49] op_sel_hi:[1,0]
	v_pk_mul_f32 v[22:23], v[4:5], s[48:49] op_sel_hi:[1,0]
	v_pk_mul_f32 v[30:31], v[6:7], s[48:49] op_sel_hi:[1,0]
	v_pk_mul_f32 v[40:41], v[8:9], s[48:49] op_sel_hi:[1,0]
	v_pk_mul_f32 v[44:45], v[10:11], s[48:49] op_sel_hi:[1,0]
	v_and_b32_sdwa v5, v12, v90 dst_sel:DWORD dst_unused:UNUSED_PAD src0_sel:WORD_1 src1_sel:DWORD
	v_and_b32_sdwa v8, v14, v90 dst_sel:DWORD dst_unused:UNUSED_PAD src0_sel:WORD_1 src1_sel:DWORD
	v_and_b32_sdwa v9, v23, v90 dst_sel:DWORD dst_unused:UNUSED_PAD src0_sel:WORD_1 src1_sel:DWORD
	v_and_b32_sdwa v11, v22, v90 dst_sel:DWORD dst_unused:UNUSED_PAD src0_sel:WORD_1 src1_sel:DWORD
	v_pk_mul_f32 v[28:29], v[16:17], s[48:49] op_sel_hi:[1,0]
	v_and_b32_sdwa v24, v30, v90 dst_sel:DWORD dst_unused:UNUSED_PAD src0_sel:WORD_1 src1_sel:DWORD
	v_add3_u32 v7, v12, v5, s97
	v_add3_u32 v12, v14, v8, s97
	v_add3_u32 v14, v23, v9, s97
; __device__ __forceinline__ bf16 f2bf(float f) { unsigned u = __float_as_uint(f); return (bf16)((u + 0x7fffu + ((u >> 16) & 1u)) >> 16); }
; __device__ __forceinline__ float sum32f(float v) { auto rr = __builtin_amdgcn_permlane32_swap(__float_as_uint(v), __float_as_uint(v), false, false); return __uint_as_float(rr[0]) + __uint_as_float(rr[1]); }
; template <int MODE, int DQK, int DV>
; __device__ __forceinline__ void attn_pass(LAS unsigned char* lds, const Tens& T, size_t rowbase, int q0, f32x16 (&o)[DV / 32], float& l_out, const int wave, QPre* qp = nullptr) {
;     ...
;                 for (int j = 0; j < 8; ++j) a[j] = (short)f2bf(__uint_as_float(((unsigned)(unsigned short)a[j]) << 16) * T.scale2);
;             }
;             qf[s] = a;
;         }
;     }
;     float ct2 = 0.f, bq = 0.f;
;     if (MODE == AM_FOX) {
;         ct2 = T.lc[(rowbase + tq) * 8] * LOG2E;
;         float qs = 0.f;
; #pragma unroll
;         for (int s = 0; s < NSTEP; ++s)
; #pragma unroll
;             for (int j = 0; j < 8; ++j) { const float v = __uint_as_float(((unsigned)(unsigned short)qf[s][j]) << 16); qs = fmaf(v, v, qs); }
;         qs = sum32f(qs);
;         bq = sqrtf(qs) * T.kmaxn * 1.001f + 1.0f;
	v_add3_u32 v16, v22, v11, s97
	v_and_b32_e32 v23, 0xffff0000, v25
	v_lshlrev_b32_e32 v22, 16, v25
	v_add3_u32 v8, v30, v24, s97
	v_pk_mul_f32 v[24:25], v[22:23], s[48:49] op_sel_hi:[1,0]
	v_pk_mul_f32 v[38:39], v[18:19], s[48:49] op_sel_hi:[1,0]
	v_and_b32_sdwa v22, v25, v90 dst_sel:DWORD dst_unused:UNUSED_PAD src0_sel:WORD_1 src1_sel:DWORD
	v_and_b32_sdwa v23, v24, v90 dst_sel:DWORD dst_unused:UNUSED_PAD src0_sel:WORD_1 src1_sel:DWORD
	v_and_b32_sdwa v17, v29, v90 dst_sel:DWORD dst_unused:UNUSED_PAD src0_sel:WORD_1 src1_sel:DWORD
	v_and_b32_sdwa v19, v28, v90 dst_sel:DWORD dst_unused:UNUSED_PAD src0_sel:WORD_1 src1_sel:DWORD
	v_add3_u32 v22, v25, v22, s97
	v_add3_u32 v23, v24, v23, s97
	v_and_b32_e32 v25, 0xffff0000, v26
	v_lshlrev_b32_e32 v24, 16, v26
	v_pk_mul_f32 v[42:43], v[20:21], s[48:49] op_sel_hi:[1,0]
	v_add3_u32 v18, v29, v17, s97
	v_add3_u32 v20, v28, v19, s97
	v_pk_mul_f32 v[28:29], v[24:25], s[48:49] op_sel_hi:[1,0]
	v_and_b32_sdwa v21, v31, v90 dst_sel:DWORD dst_unused:UNUSED_PAD src0_sel:WORD_1 src1_sel:DWORD
	v_and_b32_sdwa v24, v29, v90 dst_sel:DWORD dst_unused:UNUSED_PAD src0_sel:WORD_1 src1_sel:DWORD
	v_and_b32_sdwa v25, v28, v90 dst_sel:DWORD dst_unused:UNUSED_PAD src0_sel:WORD_1 src1_sel:DWORD
	v_add3_u32 v24, v29, v24, s97
	v_add3_u32 v25, v28, v25, s97
	v_and_b32_e32 v29, 0xffff0000, v27
	v_lshlrev_b32_e32 v28, 16, v27
	v_pk_mul_f32 v[26:27], v[28:29], s[48:49] op_sel_hi:[1,0]
	v_add3_u32 v5, v31, v21, s97
	v_and_b32_sdwa v28, v27, v90 dst_sel:DWORD dst_unused:UNUSED_PAD src0_sel:WORD_1 src1_sel:DWORD
	v_and_b32_sdwa v29, v26, v90 dst_sel:DWORD dst_unused:UNUSED_PAD src0_sel:WORD_1 src1_sel:DWORD
	v_add3_u32 v28, v27, v28, s97
	v_add3_u32 v29, v26, v29, s97
	v_and_b32_e32 v27, 0xffff0000, v32
	v_lshlrev_b32_e32 v26, 16, v32
	v_pk_mul_f32 v[30:31], v[26:27], s[48:49] op_sel_hi:[1,0]
	v_and_b32_sdwa v4, v13, v90 dst_sel:DWORD dst_unused:UNUSED_PAD src0_sel:WORD_1 src1_sel:DWORD
	v_and_b32_sdwa v26, v31, v90 dst_sel:DWORD dst_unused:UNUSED_PAD src0_sel:WORD_1 src1_sel:DWORD
	v_and_b32_sdwa v27, v30, v90 dst_sel:DWORD dst_unused:UNUSED_PAD src0_sel:WORD_1 src1_sel:DWORD
	v_add3_u32 v26, v31, v26, s97
	v_add3_u32 v27, v30, v27, s97
	v_and_b32_e32 v31, 0xffff0000, v33
	v_lshlrev_b32_e32 v30, 16, v33
	v_pk_mul_f32 v[32:33], v[30:31], s[48:49] op_sel_hi:[1,0]
	v_and_b32_sdwa v47, v39, v90 dst_sel:DWORD dst_unused:UNUSED_PAD src0_sel:WORD_1 src1_sel:DWORD
	v_and_b32_sdwa v30, v33, v90 dst_sel:DWORD dst_unused:UNUSED_PAD src0_sel:WORD_1 src1_sel:DWORD
	v_and_b32_sdwa v31, v32, v90 dst_sel:DWORD dst_unused:UNUSED_PAD src0_sel:WORD_1 src1_sel:DWORD
	v_and_b32_sdwa v48, v38, v90 dst_sel:DWORD dst_unused:UNUSED_PAD src0_sel:WORD_1 src1_sel:DWORD
	v_add3_u32 v30, v33, v30, s97
	v_add3_u32 v31, v32, v31, s97
	v_and_b32_e32 v33, 0xffff0000, v34
	v_lshlrev_b32_e32 v32, 16, v34
	v_add3_u32 v4, v13, v4, s97
	v_add3_u32 v11, v39, v47, s97
	v_add3_u32 v13, v38, v48, s97
	v_pk_mul_f32 v[38:39], v[32:33], s[48:49] op_sel_hi:[1,0]
	v_and_b32_e32 v37, 0xffff0000, v7
	v_and_b32_sdwa v32, v39, v90 dst_sel:DWORD dst_unused:UNUSED_PAD src0_sel:WORD_1 src1_sel:DWORD
	v_and_b32_sdwa v33, v38, v90 dst_sel:DWORD dst_unused:UNUSED_PAD src0_sel:WORD_1 src1_sel:DWORD
	v_add3_u32 v32, v39, v32, s97
	v_add3_u32 v33, v38, v33, s97
	v_and_b32_e32 v39, 0xffff0000, v35
	v_lshlrev_b32_e32 v38, 16, v35
	v_pk_mul_f32 v[38:39], v[38:39], s[48:49] op_sel_hi:[1,0]
	v_and_b32_sdwa v6, v15, v90 dst_sel:DWORD dst_unused:UNUSED_PAD src0_sel:WORD_1 src1_sel:DWORD
	v_and_b32_sdwa v35, v38, v90 dst_sel:DWORD dst_unused:UNUSED_PAD src0_sel:WORD_1 src1_sel:DWORD
	v_add3_u32 v35, v38, v35, s97
	v_fma_f32 v37, v37, v37, 0
	v_and_b32_e32 v38, 0xffff0000, v4
	v_add3_u32 v10, v15, v6, s97
	v_fmac_f32_e32 v37, v38, v38
	v_and_b32_e32 v38, 0xffff0000, v12
	v_fmac_f32_e32 v37, v38, v38
	v_and_b32_e32 v38, 0xffff0000, v10
	v_fmac_f32_e32 v37, v38, v38
	v_and_b32_e32 v38, 0xffff0000, v16
	v_fmac_f32_e32 v37, v38, v38
	v_and_b32_e32 v38, 0xffff0000, v14
	v_fmac_f32_e32 v37, v38, v38
	v_and_b32_e32 v38, 0xffff0000, v20
	v_fmac_f32_e32 v37, v38, v38
	v_and_b32_e32 v38, 0xffff0000, v18
	v_fmac_f32_e32 v37, v38, v38
	v_and_b32_e32 v38, 0xffff0000, v8
	v_fmac_f32_e32 v37, v38, v38
	v_and_b32_e32 v38, 0xffff0000, v5
	v_and_b32_sdwa v50, v40, v90 dst_sel:DWORD dst_unused:UNUSED_PAD src0_sel:WORD_1 src1_sel:DWORD
	v_fmac_f32_e32 v37, v38, v38
	v_and_b32_e32 v38, 0xffff0000, v13
	v_and_b32_sdwa v49, v41, v90 dst_sel:DWORD dst_unused:UNUSED_PAD src0_sel:WORD_1 src1_sel:DWORD
	v_add3_u32 v17, v40, v50, s97
	v_fmac_f32_e32 v37, v38, v38
	v_and_b32_e32 v38, 0xffff0000, v11
	v_and_b32_sdwa v52, v42, v90 dst_sel:DWORD dst_unused:UNUSED_PAD src0_sel:WORD_1 src1_sel:DWORD
	v_add3_u32 v15, v41, v49, s97
	v_fmac_f32_e32 v37, v38, v38
	v_and_b32_e32 v38, 0xffff0000, v17
	v_and_b32_sdwa v51, v43, v90 dst_sel:DWORD dst_unused:UNUSED_PAD src0_sel:WORD_1 src1_sel:DWORD
	v_add3_u32 v21, v42, v52, s97
	v_fmac_f32_e32 v37, v38, v38
	v_and_b32_e32 v38, 0xffff0000, v15
	v_and_b32_sdwa v54, v44, v90 dst_sel:DWORD dst_unused:UNUSED_PAD src0_sel:WORD_1 src1_sel:DWORD
	v_add3_u32 v19, v43, v51, s97
	v_and_b32_sdwa v34, v39, v90 dst_sel:DWORD dst_unused:UNUSED_PAD src0_sel:WORD_1 src1_sel:DWORD
	v_fmac_f32_e32 v37, v38, v38
	v_and_b32_e32 v38, 0xffff0000, v21
	v_and_b32_sdwa v53, v45, v90 dst_sel:DWORD dst_unused:UNUSED_PAD src0_sel:WORD_1 src1_sel:DWORD
	v_add3_u32 v9, v44, v54, s97
	v_add3_u32 v34, v39, v34, s97
	v_fmac_f32_e32 v37, v38, v38
	v_and_b32_e32 v38, 0xffff0000, v19
	v_add3_u32 v6, v45, v53, s97
	v_fmac_f32_e32 v37, v38, v38
	v_and_b32_e32 v38, 0xffff0000, v9
	v_fmac_f32_e32 v37, v38, v38
	v_and_b32_e32 v38, 0xffff0000, v6
	v_fmac_f32_e32 v37, v38, v38
	v_and_b32_e32 v38, 0xffff0000, v23
	v_fmac_f32_e32 v37, v38, v38
	v_and_b32_e32 v38, 0xffff0000, v22
	v_fmac_f32_e32 v37, v38, v38
	v_and_b32_e32 v38, 0xffff0000, v25
	v_fmac_f32_e32 v37, v38, v38
	v_and_b32_e32 v38, 0xffff0000, v24
	v_fmac_f32_e32 v37, v38, v38
	v_and_b32_e32 v38, 0xffff0000, v29
	v_fmac_f32_e32 v37, v38, v38
	v_and_b32_e32 v38, 0xffff0000, v28
	v_fmac_f32_e32 v37, v38, v38
	v_and_b32_e32 v38, 0xffff0000, v27
	v_fmac_f32_e32 v37, v38, v38
	v_and_b32_e32 v38, 0xffff0000, v26
	v_fmac_f32_e32 v37, v38, v38
	v_and_b32_e32 v38, 0xffff0000, v31
	v_fmac_f32_e32 v37, v38, v38
	v_and_b32_e32 v38, 0xffff0000, v30
	v_fmac_f32_e32 v37, v38, v38
	v_and_b32_e32 v38, 0xffff0000, v33
	v_fmac_f32_e32 v37, v38, v38
	v_and_b32_e32 v38, 0xffff0000, v32
	v_fmac_f32_e32 v37, v38, v38
	v_and_b32_e32 v38, 0xffff0000, v35
	v_fmac_f32_e32 v37, v38, v38
	v_and_b32_e32 v38, 0xffff0000, v34
	v_fmac_f32_e32 v37, v38, v38
	v_mov_b32_e32 v38, v37
	s_nop 1
	v_permlane32_swap_b32_e32 v37, v38
	s_and_b64 vcc, exec, s[12:13]
	s_cbranch_vccnz .LBB0_635
	s_lshl_b64 s[2:3], s[44:45], 11
	s_add_u32 s2, s9, s2
	s_addc_u32 s3, s10, s3
	v_readlane_b32 s12, v254, 57
	s_mov_b32 m0, s12
	s_nop 0
	global_load_lds_dword v99, s[2:3]

; template <int MODE, int DQK, int DV>
; __device__ __forceinline__ void attn_pass(LAS unsigned char* lds, const Tens& T, size_t rowbase, int q0, f32x16 (&o)[DV / 32], float& l_out, const int wave, QPre* qp = nullptr) {
;     ...
;     const unsigned lds0 = (unsigned)(uintptr_t)lds;
;     ...
;     const unsigned kvo = (unsigned)(dk_key * T.ldk + dk_col) * 2u, rvo = (unsigned)(dr_key * T.ldk2 + dr_col) * 2u;
;     unsigned vvo[DV / 64];
; #pragma unroll
;     for (int n = 0; n < DV / 64; ++n) vvo[n] = (unsigned)(dv_key[n] * T.ldv + dv_col[n]) * 2u;
;     const unsigned cvo = (unsigned)lane * 32u, mvo = (unsigned)(wave * 64 + lane) * 4u;
;     const char* const ubK = (const char*)(T.K + rowbase * (size_t)T.ldk);
;     const char* const ubK2 = (MODE == AM_MLA) ? (const char*)(T.K2 + rowbase * (size_t)T.ldk2) : nullptr;
;     const char* const ubV = (const char*)(T.V + rowbase * (size_t)T.ldv);
;     const char* const ubC = (MODE == AM_FOX) ? (const char*)(T.lc + rowbase * 8) : nullptr;
;     const char* const ubM = (MODE == AM_DSA) ? (const char*)(T.mask + ((rowbase / S * 128) * (size_t)S + q0) * 2) : nullptr;
;     ...
;     const int nvm = 1 + ((DQK == 96 && wave < 4) ? 1 : 0) + DV / 64 + ((MODE == AM_FOX && wave == 0) ? 1 : 0) + ((MODE == AM_DSA) ? 1 : 0);
;     ...
;     const unsigned koff = (unsigned)(r * 128), kswz = (unsigned)((r >> 1) & 7);
;     const unsigned roff = (unsigned)(8192 + r * 64), rswz = (unsigned)((r >> 2) & 3);
;     const int g16 = lane >> 4, qq = (lane & 15) >> 2, pp = lane & 3;
; template <int PH>
; __device__ __forceinline__ void mk_body(const Args& a) {
;     ...
;             const int b = u >> 8, h = (u >> 5) & 7, qb = 31 - (u & 31);
;             { const int t_ = wave * 64 + lane_id_v();
;               if (t_ <= 128) ((LAS float*)(lds + att::OFF_LUT))[t_] = (t_ < 128) ? (t5[bucket_tab[t_] * 8 + h] - t5[31 * 8 + h]) * att::LOG2E : 0.f;
;               if (t_ >= 192 && t_ < 256) { const int e_ = (t_ - 192) >> 2, c_ = t_ & 3; ((LAS float*)(lds + att::OFF_LUT + 768))[t_ - 192] = ((e_ >> c_) & 1) ? 0.f : -INFINITY; } }
;             att::Tens T{};
;             T.Q = y0 + Y0_DQ + h * 64; T.ldq = Y0P; T.K = y0 + Y0_DK + h * 64; T.ldk = Y0P; T.V = y0 + Y0_DV + h * 64; T.ldv = Y0P;
;             T.mask = maskg; T.scale2 = 0.125f * att::LOG2E;
;             att::f32x16 o[2]; float l;
;             att::attn_pass<att::AM_DSA, 64, 64>(lds, T, (size_t)b * S, qb * 256, o, l, wave, &qp);
.LBB0_1618:
	s_lshr_b32 s12, s8, 8
	s_lshl_b32 s0, s0, 8
	s_add_u32 s16, s6, s0
	s_addc_u32 s17, s7, 0
	s_lshl_b32 s81, s1, 6
	s_lshl_b32 s0, s1, 7
	s_add_u32 s10, s92, s0
	s_addc_u32 s11, s40, 0
	s_add_u32 s1, s41, s0
	s_addc_u32 s2, s44, 0
	s_add_u32 s3, s45, s0
	s_addc_u32 s4, s46, 0
	s_not_b32 s0, s8
	s_lshl_b32 s0, s0, 8
	s_and_b32 s82, s0, 0x1f00
	v_mbcnt_lo_u32_b32 v28, -1, 0
	v_mbcnt_hi_u32_b32 v28, -1, v28
	s_add_i32 s83, s82, s49
	v_and_b32_e32 v29, 31, v28
	s_lshl_b64 s[18:19], s[12:13], 13
	v_or_b32_e32 v0, s83, v29
	v_mov_b32_e32 v1, v66
	v_lshl_add_u64 v[0:1], s[18:19], 0, v[0:1]
	v_mov_b64_e32 v[2:3], s[10:11]
	s_movk_i32 s0, 0x1c00
	v_bfe_u32 v30, v28, 5, 1
	v_mad_u64_u32 v[2:3], s[8:9], v0, s0, v[2:3]
	v_mad_u32_u24 v3, v1, s0, v3
	v_lshlrev_b32_e32 v0, 4, v30
	v_mov_b32_e32 v1, v66
	v_lshl_add_u64 v[12:13], v[2:3], 0, v[0:1]
	global_load_dwordx4 v[0:3], v[12:13], off
	global_load_dwordx4 v[4:7], v[12:13], off offset:32
	global_load_dwordx4 v[8:11], v[12:13], off offset:64
	s_movk_i32 s5, 0xe00
	global_load_dwordx4 v[12:15], v[12:13], off offset:96
	s_add_i32 s0, s82, 0x100
	s_lshl_b64 s[8:9], s[12:13], 23
	s_mul_i32 s11, s12, 0x3800000
	s_mul_hi_u32 s10, s12, 0x3800000
	v_and_b32_e32 v31, 63, v28
	v_lshlrev_b32_e32 v106, 2, v30
	v_lshlrev_b32_e32 v105, 3, v29
	s_mov_b32 s84, 4
	v_mov_b32_e32 v65, v66
	v_mov_b32_e32 v67, v66
	v_mov_b32_e32 v70, v66
	v_mov_b32_e32 v71, v66
	v_or_b32_e32 v107, 8, v106
	v_or_b32_e32 v108, 16, v106
	v_or_b32_e32 v109, 24, v106
	v_mov_b32_e32 v111, 0
	v_mov_b32_e32 v112, 0xc2800000
	v_mov_b32_e32 v103, 0
	s_mov_b64 s[26:27], 0
	v_bfe_u32 v220, v28, 3, 3
	v_or_b32_e32 v221, s64, v220
	v_lshrrev_b32_e32 v222, 4, v28
	v_lshrrev_b32_e32 v223, 2, v28
	v_lshrrev_b32_e32 v224, 1, v221
	v_xor_b32_e32 v225, v223, v222
	v_xor_b32_e32 v226, v224, v28
	v_lshlrev_b32_e32 v227, 5, v225
	v_lshlrev_b32_e32 v228, 3, v28
	v_mul_lo_u32 v229, v221, s5
	s_lshl_b32 s5, s82, 3
	v_lshlrev_b32_e32 v230, 3, v226
	v_and_b32_e32 v231, 32, v227
	v_and_b32_e32 v232, 24, v228
	s_add_u32 s20, s3, s11
	v_and_or_b32 v233, v230, 56, v229
	v_or3_b32 v234, v232, v231, v229
	s_addc_u32 s21, s4, s10
	v_lshlrev_b32_e32 v95, 1, v234
	v_lshlrev_b32_e32 v235, 2, v31
	v_lshrrev_b32_e32 v236, 1, v28
	v_bfe_u32 v237, v28, 1, 3
	v_bfe_u32 v238, v28, 2, 2
	v_and_b32_e32 v28, 16, v28
	s_add_u32 s22, s1, s11
	v_and_or_b32 v239, v220, 4, v238
	v_and_or_b32 v28, v235, 12, v28
	v_lshl_add_u32 v240, v29, 7, 0
	v_bitop3_b32 v241, v30, v236, 7 bitop3:0x78
	s_addc_u32 s23, s2, s10
	v_lshl_add_u32 v96, v241, 4, v240
	v_bitop3_b32 v242, v30, v237, 2 bitop3:0x36
	v_or_b32_e32 v100, s65, v235
	v_lshlrev_b32_e32 v243, 7, v239
	v_lshlrev_b32_e32 v244, 1, v28
	s_add_u32 s1, s47, s8
	v_lshl_add_u32 v97, v242, 4, v240
	v_bitop3_b32 v245, v30, v237, 4 bitop3:0x36
	v_add3_u32 v246, 0, v243, v244
	v_and_b32_e32 v247, 64, v228
	s_mov_b32 s3, 0xc000
	s_addc_u32 s2, s48, s9
	v_lshl_add_u32 v98, v245, 4, v240
	v_bitop3_b32 v248, v30, v237, 6 bitop3:0x36
	v_add3_u32 v101, v246, v247, s3
	v_bitop3_b32 v249, v228, 64, v228 bitop3:0xc
	s_add_u32 s24, s1, s5
	v_lshl_add_u32 v99, v248, 4, v240
	v_add3_u32 v102, v246, v249, s3
	s_addc_u32 s25, s2, 0
	s_add_i32 s85, s66, 0
	v_lshlrev_b32_e32 v104, 1, v233
	s_lshr_b32 s12, s83, 6
	s_mov_b32 m0, s85
	s_nop 0
	global_load_lds_dwordx4 v104, s[22:23]
	s_add_i32 s88, s85, 0xc000
	s_mov_b32 m0, s88
	s_nop 0
	global_load_lds_dwordx4 v95, s[20:21]
	s_add_u32 s2, s22, 0x70000
	s_mov_b32 m0, s67
	s_nop 0
	global_load_lds_dword v100, s[24:25]
	s_addc_u32 s3, s23, 0
	s_add_i32 s89, s85, 0x2000
	s_mov_b32 m0, s89
	s_nop 0
	global_load_lds_dwordx4 v104, s[2:3]
	s_add_u32 s2, s20, 0x70000
	s_addc_u32 s3, s21, 0
	s_add_i32 s91, s85, 0xe000
	s_mov_b32 m0, s91
	s_nop 0
	global_load_lds_dwordx4 v95, s[2:3]
	s_add_u32 s2, s24, 0x10000
	s_addc_u32 s3, s25, 0
	s_mov_b32 m0, s68
	s_nop 0
	global_load_lds_dword v100, s[2:3]
	s_add_u32 s2, s22, 0xe0000
	s_addc_u32 s3, s23, 0
	s_add_i32 s93, s85, 0x4000
	s_mov_b32 m0, s93
	s_nop 0
	global_load_lds_dwordx4 v104, s[2:3]
	s_add_u32 s2, s20, 0xe0000
	s_addc_u32 s3, s21, 0
	s_add_i32 s94, s85, 0x10000
	s_mov_b32 m0, s94
	s_nop 0
	global_load_lds_dwordx4 v95, s[2:3]
	s_add_u32 s2, s24, 0x20000
	s_addc_u32 s3, s25, 0
	s_mov_b32 m0, s69
	s_nop 0
	global_load_lds_dword v100, s[2:3]
	s_add_u32 s2, s22, 0x150000
	s_addc_u32 s3, s23, 0
	s_add_i32 s95, s85, 0x6000
	s_mov_b32 m0, s95
	s_nop 0
	global_load_lds_dwordx4 v104, s[2:3]
	s_add_u32 s2, s20, 0x150000
	s_addc_u32 s3, s21, 0
	s_add_i32 s96, s85, 0x12000
	s_mov_b32 m0, s96
	s_nop 0
	global_load_lds_dwordx4 v95, s[2:3]
	s_add_u32 s2, s24, 0x30000
	s_addc_u32 s3, s25, 0
	s_mov_b32 m0, s70
	s_nop 0
	global_load_lds_dword v100, s[2:3]
	s_lshr_b32 s97, s0, 7
	s_add_i32 s8, s83, 0xffffff01
	s_add_i32 s1, s73, s82
	s_waitcnt vmcnt(12)
; #define LAS __attribute__((address_space(3)))
; __device__ __forceinline__ bf16 f2bf(float f) { unsigned u = __float_as_uint(f); return (bf16)((u + 0x7fffu + ((u >> 16) & 1u)) >> 16); }
; #define ATT_ISSUE(st_, sl) do { _Pragma("unroll") for (int sb_ = 0; sb_ < NSUB; ++sb_) ATT_DMA(ATT_TILE((st_) * NSUB + sb_), sl, sb_); } while (0)
; template <int MODE, int DQK, int DV>
; __device__ __forceinline__ void attn_pass(LAS unsigned char* lds, const Tens& T, size_t rowbase, int q0, f32x16 (&o)[DV / 32], float& l_out, const int wave, QPre* qp = nullptr) {
;     ...
;         for (int s = 0; s < NSTEP; ++s) {
;             if (MODE == AM_MLA && s == NSTEP - 1) continue;
;             bf16x8 a = qf[s];
;             if (MODE == AM_MLA && s == NSTEP - 2) {
;                 bf16x8 b2 = qf[NSTEP - 1];
; #pragma unroll
;                 for (int j = 0; j < 8; ++j) {
;                     const float x1 = __uint_as_float(((unsigned)(unsigned short)a[j]) << 16), x2 = __uint_as_float(((unsigned)(unsigned short)b2[j]) << 16);
;                     const float cs = j < 4 ? c0[j & 3] : c1[j & 3], sn = j < 4 ? s0[j & 3] : s1[j & 3];
;                     a[j] = (short)f2bf((x1 * cs - x2 * sn) * T.scale2); b2[j] = (short)f2bf((x2 * cs + x1 * sn) * T.scale2);
;                 }
;                 qf[NSTEP - 1] = b2;
;             } else {
; #pragma unroll
;                 for (int j = 0; j < 8; ++j) a[j] = (short)f2bf(__uint_as_float(((unsigned)(unsigned short)a[j]) << 16) * T.scale2);
;             }
;             qf[s] = a;
;         }
;     ...
;     float m = -64.0f, l = 0.f;
;     bf16x8 kone = {0, 0, 0, 0, 0, 0, 0, 0}, qm = kone;
;     if (MODE == AM_DSA) { if (h == 0) { kone[0] = (short)0x3F80; kone[1] = (short)0x3F80; kone[2] = (short)0x3F80; } qm = split3_bf16(64.0f, h); }
;     f32x16 negm;
; #pragma unroll
;     for (int rg = 0; rg < 16; ++rg) negm[rg] = 64.0f;
; #pragma unroll
;     for (int i = 0; i < NDB; ++i) o[i] = f32x16{};
;     const int jlast = (q0 + wave * 32) / 64;
;     constexpr bool DESC = (MODE == AM_FOX);
;     ...
;     bool wdone = false;
;     volatile LAS int* dflag = (volatile LAS int*)(lds + OFF_MISC + 16);
;     const int nst = ntile / NSUB;
;     ATT_ISSUE(0, 0);
;     if (NRING == 3) ATT_ISSUE(1, 1);
;     if (NRING == 3) ATT_WAIT_PREV(); else asm volatile("s_waitcnt vmcnt(0)" ::: "memory");
;     ATT_BAR();
	v_and_b32_e32 v17, 0xffff0000, v0
	v_lshlrev_b32_e32 v16, 16, v0
	v_and_b32_e32 v19, 0xffff0000, v1
	v_lshlrev_b32_e32 v18, 16, v1
	v_and_b32_e32 v1, 0xffff0000, v2
	v_lshlrev_b32_e32 v0, 16, v2
	v_and_b32_e32 v21, 0xffff0000, v3
	v_lshlrev_b32_e32 v20, 16, v3
	v_and_b32_e32 v3, 0xffff0000, v4
	v_lshlrev_b32_e32 v2, 16, v4
	v_and_b32_e32 v25, 0xffff0000, v7
	v_lshlrev_b32_e32 v24, 16, v7
	v_pk_mul_f32 v[20:21], v[20:21], s[14:15] op_sel_hi:[1,0]
	v_pk_mul_f32 v[2:3], v[2:3], s[14:15] op_sel_hi:[1,0]
	v_and_b32_e32 v23, 0xffff0000, v5
	v_lshlrev_b32_e32 v22, 16, v5
	v_and_b32_e32 v5, 0xffff0000, v6
	v_lshlrev_b32_e32 v4, 16, v6
	v_and_b32_e32 v7, 0xffff0000, v8
	v_lshlrev_b32_e32 v6, 16, v8
	v_and_b32_e32 v27, 0xffff0000, v9
	v_lshlrev_b32_e32 v26, 16, v9
	v_and_b32_e32 v9, 0xffff0000, v10
	v_lshlrev_b32_e32 v8, 16, v10
	v_pk_mul_f32 v[16:17], v[16:17], s[14:15] op_sel_hi:[1,0]
	v_pk_mul_f32 v[24:25], v[24:25], s[14:15] op_sel_hi:[1,0]
	v_bfe_u32 v10, v21, 16, 1
	v_bfe_u32 v32, v20, 16, 1
	v_bfe_u32 v45, v3, 16, 1
	v_bfe_u32 v46, v2, 16, 1
	v_pk_mul_f32 v[18:19], v[18:19], s[14:15] op_sel_hi:[1,0]
	v_pk_mul_f32 v[0:1], v[0:1], s[14:15] op_sel_hi:[1,0]
	v_pk_mul_f32 v[4:5], v[4:5], s[14:15] op_sel_hi:[1,0]
	v_pk_mul_f32 v[6:7], v[6:7], s[14:15] op_sel_hi:[1,0]
	v_bfe_u32 v38, v16, 16, 1
	v_bfe_u32 v39, v25, 16, 1
	v_add3_u32 v20, v20, v32, s76
	v_add3_u32 v10, v21, v10, s76
	v_add3_u32 v21, v2, v46, s76
	v_add3_u32 v32, v3, v45, s76
	v_and_b32_e32 v3, 0xffff0000, v11
	v_lshlrev_b32_e32 v2, 16, v11
	v_pk_mul_f32 v[26:27], v[26:27], s[14:15] op_sel_hi:[1,0]
	v_bfe_u32 v33, v1, 16, 1
	v_bfe_u32 v34, v0, 16, 1
	v_bfe_u32 v35, v19, 16, 1
	v_bfe_u32 v36, v18, 16, 1
	v_bfe_u32 v37, v17, 16, 1
	v_bfe_u32 v41, v5, 16, 1
	v_bfe_u32 v42, v4, 16, 1
	v_add3_u32 v16, v16, v38, s76
	v_add3_u32 v25, v25, v39, s76
	v_pk_mul_f32 v[2:3], v[2:3], s[14:15] op_sel_hi:[1,0]
	v_bfe_u32 v38, v7, 16, 1
	v_bfe_u32 v39, v6, 16, 1
	v_add3_u32 v17, v17, v37, s76
	v_add3_u32 v18, v18, v36, s76
	v_add3_u32 v19, v19, v35, s76
	v_add3_u32 v34, v0, v34, s76
	v_add3_u32 v33, v1, v33, s76
	v_add3_u32 v35, v4, v42, s76
	v_add3_u32 v36, v5, v41, s76
	v_pk_mul_f32 v[0:1], v[8:9], s[14:15] op_sel_hi:[1,0]
	v_bfe_u32 v4, v3, 16, 1
	v_bfe_u32 v5, v2, 16, 1
	v_bfe_u32 v11, v27, 16, 1
	v_bfe_u32 v37, v26, 16, 1
	v_add3_u32 v39, v6, v39, s76
	v_add3_u32 v38, v7, v38, s76
	v_and_b32_e32 v7, 0xffff0000, v15
	v_lshlrev_b32_e32 v6, 16, v15
	v_bfe_u32 v8, v1, 16, 1
	v_bfe_u32 v9, v0, 16, 1
	v_add3_u32 v26, v26, v37, s76
	v_add3_u32 v11, v27, v11, s76
	v_add3_u32 v27, v2, v5, s76
	v_add3_u32 v37, v3, v4, s76
	v_and_b32_e32 v3, 0xffff0000, v13
	v_lshlrev_b32_e32 v2, 16, v13
	v_and_b32_e32 v5, 0xffff0000, v14
	v_lshlrev_b32_e32 v4, 16, v14
	v_pk_mul_f32 v[6:7], v[6:7], s[14:15] op_sel_hi:[1,0]
	v_bfe_u32 v40, v24, 16, 1
	v_add3_u32 v9, v0, v9, s76
	v_add3_u32 v8, v1, v8, s76
	v_and_b32_e32 v1, 0xffff0000, v12
	v_lshlrev_b32_e32 v0, 16, v12
	v_pk_mul_f32 v[2:3], v[2:3], s[14:15] op_sel_hi:[1,0]
	v_pk_mul_f32 v[4:5], v[4:5], s[14:15] op_sel_hi:[1,0]
	v_bfe_u32 v12, v7, 16, 1
	v_add3_u32 v24, v24, v40, s76
	v_bfe_u32 v13, v6, 16, 1
	v_bfe_u32 v15, v4, 16, 1
	v_bfe_u32 v40, v3, 16, 1
	v_add3_u32 v7, v7, v12, s76
	v_bfe_u32 v14, v5, 16, 1
	v_add3_u32 v3, v3, v40, s76
	v_add3_u32 v4, v4, v15, s76
	v_add3_u32 v6, v6, v13, s76
	v_add3_u32 v5, v5, v14, s76
	v_bfe_u32 v41, v2, 16, 1
	v_pk_mul_f32 v[0:1], v[0:1], s[14:15] op_sel_hi:[1,0]
	v_add3_u32 v2, v2, v41, s76
	v_bfe_u32 v42, v1, 16, 1
	v_add3_u32 v1, v1, v42, s76
	v_pk_mul_f32 v[22:23], v[22:23], s[14:15] op_sel_hi:[1,0]
	v_bfe_u32 v43, v23, 16, 1
	v_add3_u32 v23, v23, v43, s76
	v_bfe_u32 v43, v0, 16, 1
	v_bfe_u32 v44, v22, 16, 1
	v_add3_u32 v0, v0, v43, s76
	s_waitcnt vmcnt(6)
	s_add_u32 s24, s24, 0x90000
	v_add3_u32 v22, v22, v44, s76
	s_waitcnt lgkmcnt(0)
	s_barrier
	v_or_b32_e32 v12, s90, v31
	v_perm_b32 v72, v17, v16, s78
	v_perm_b32 v84, v1, v0, s78
	v_add_u32_e32 v0, s1, v29
	s_addc_u32 s25, s25, 0
	s_lshr_b32 s0, s0, 6
	v_mov_b32_e32 v16, v66
	v_mov_b32_e32 v17, v66
	v_cmp_gt_u32_e64 s[2:3], 32, v31
	v_cmp_ne_u32_e64 s[4:5], 0, v12
	v_perm_b32 v75, v10, v20, s78
	v_perm_b32 v73, v19, v18, s78
	v_perm_b32 v79, v25, v24, s78
	v_perm_b32 v77, v23, v22, s78
	v_perm_b32 v76, v32, v21, s78
	v_perm_b32 v83, v37, v27, s78
	v_perm_b32 v82, v8, v9, s78
	v_perm_b32 v81, v11, v26, s78
	v_perm_b32 v87, v7, v6, s78
	v_perm_b32 v86, v5, v4, s78
	v_perm_b32 v85, v3, v2, s78
	v_sub_u32_e32 v110, v0, v106
	s_mul_i32 s0, s0, 0x70000
	v_mov_b32_e32 v18, v66
	v_mov_b32_e32 v19, v66
	v_mov_b32_e32 v20, v66
	v_mov_b32_e32 v21, v66
	v_mov_b32_e32 v22, v66
	v_mov_b32_e32 v23, v66
	v_mov_b32_e32 v24, v66
	v_mov_b32_e32 v25, v66
	v_mov_b32_e32 v26, v66
	v_mov_b32_e32 v27, v66
	v_mov_b32_e32 v28, v66
	v_mov_b32_e32 v29, v66
	v_mov_b32_e32 v30, v66
	v_mov_b32_e32 v31, v66
	v_mov_b64_e32 v[0:1], v[16:17]
	v_cndmask_b32_e64 v64, 0, v90, s[2:3]
	s_mov_b32 s10, 0
	v_cndmask_b32_e64 v69, 0, v91, s[2:3]
	v_cndmask_b32_e64 v68, 0, v92, s[2:3]
	v_perm_b32 v74, v33, v34, s78
	v_perm_b32 v78, v36, v35, s78
	v_perm_b32 v80, v38, v39, s78
	s_add_u32 s9, s0, 0xffd60000
	s_add_u32 s75, s0, 0xffe40000
	s_add_u32 s77, s0, 0xffc80000
	s_mov_b32 s11, 0
	v_mov_b64_e32 v[2:3], v[18:19]
	v_mov_b64_e32 v[4:5], v[20:21]
	v_mov_b64_e32 v[6:7], v[22:23]
	v_mov_b64_e32 v[8:9], v[24:25]
	v_mov_b64_e32 v[10:11], v[26:27]
	v_mov_b64_e32 v[12:13], v[28:29]
	v_mov_b64_e32 v[14:15], v[30:31]
	s_branch .LBB0_1621

; #define LAS __attribute__((address_space(3)))
; template <int MODE, int DQK, int DV>
; __device__ __forceinline__ void attn_pass(LAS unsigned char* lds, const Tens& T, size_t rowbase, int q0, f32x16 (&o)[DV / 32], float& l_out, const int wave, QPre* qp = nullptr) {
;     ...
;     const int tq = q0 + wave * 32 + r;
;     const int ntile = (q0 + 256) / 64;
;     bf16x8 qf[NSTEP];
;     {
;         const bf16* qp = T.Q + (rowbase + tq) * (size_t)T.ldq + 8 * h;
; #pragma unroll
;         for (int s = 0; s < NSTEP; ++s) qf[s] = *(const bf16x8*)(qp + 16 * s);
;     }
;     ...
;     const unsigned lds0 = (unsigned)(uintptr_t)lds;
;     ...
;     const unsigned kvo = (unsigned)(dk_key * T.ldk + dk_col) * 2u, rvo = (unsigned)(dr_key * T.ldk2 + dr_col) * 2u;
;     unsigned vvo[DV / 64];
; #pragma unroll
;     for (int n = 0; n < DV / 64; ++n) vvo[n] = (unsigned)(dv_key[n] * T.ldv + dv_col[n]) * 2u;
;     const unsigned cvo = (unsigned)lane * 32u, mvo = (unsigned)(wave * 64 + lane) * 4u;
;     const char* const ubK = (const char*)(T.K + rowbase * (size_t)T.ldk);
;     const char* const ubK2 = (MODE == AM_MLA) ? (const char*)(T.K2 + rowbase * (size_t)T.ldk2) : nullptr;
;     const char* const ubV = (const char*)(T.V + rowbase * (size_t)T.ldv);
;     const char* const ubC = (MODE == AM_FOX) ? (const char*)(T.lc + rowbase * 8) : nullptr;
;     const char* const ubM = (MODE == AM_DSA) ? (const char*)(T.mask + ((rowbase / S * 128) * (size_t)S + q0) * 2) : nullptr;
;     ...
;     const int nvm = 1 + ((DQK == 96 && wave < 4) ? 1 : 0) + DV / 64 + ((MODE == AM_FOX && wave == 0) ? 1 : 0) + ((MODE == AM_DSA) ? 1 : 0);
;     ...
;     const unsigned koff = (unsigned)(r * 128), kswz = (unsigned)((r >> 1) & 7);
;     const unsigned roff = (unsigned)(8192 + r * 64), rswz = (unsigned)((r >> 2) & 3);
;     const int g16 = lane >> 4, qq = (lane & 15) >> 2, pp = lane & 3;
;     const int vsw = (DV == 64) ? ((qq >> 1) & 1) : qq;
;     const unsigned voff = (unsigned)((4 * (g16 >> 1) + qq) * VROW + (16 * (g16 & 1) + 4 * pp) * 2);
;     const LAS unsigned char* kfa[NSTEP]; const LAS unsigned char* vfa[NDB];
; #pragma unroll
;     for (int s = 0; s < NSTEP; ++s) {
;         kfa[s] = (s < 4) ? lds + OFF_K + koff + (((unsigned)(2 * s + h) ^ kswz) * 16) : lds + OFF_K + roff + (((unsigned)(2 * (s - 4) + h) ^ rswz) * 16);
;         asm volatile("" : "+v"(kfa[s]));
;     }
; #pragma unroll
.LBB0_2438:
	s_or_b64 exec, exec, s[4:5]
	v_mbcnt_lo_u32_b32 v1, -1, 0
	v_mbcnt_hi_u32_b32 v1, -1, v1
	s_xor_b64 s[60:61], s[2:3], -1
	v_and_b32_e32 v32, 31, v1
	s_lshl_b32 s0, s34, 7
	v_or_b32_e32 v144, s95, v32
	s_add_u32 s2, s45, s0
	v_lshl_add_u64 v[2:3], s[46:47], 0, v[144:145]
	s_addc_u32 s3, s74, 0
	v_bfe_u32 v33, v1, 5, 1
	v_lshlrev_b64 v[2:3], 12, v[2:3]
	v_lshl_add_u64 v[2:3], s[2:3], 0, v[2:3]
	v_lshlrev_b32_e32 v4, 4, v33
	v_mov_b32_e32 v5, v145
	v_lshl_add_u64 v[14:15], v[2:3], 0, v[4:5]
	global_load_dwordx4 v[2:5], v[14:15], off
	global_load_dwordx4 v[6:9], v[14:15], off offset:32
	global_load_dwordx4 v[10:13], v[14:15], off offset:64
	s_nop 0
	global_load_dwordx4 v[14:17], v[14:15], off offset:96
	s_movk_i32 s1, 0x70
	s_add_u32 s64, s96, s0
	s_addc_u32 s65, s97, 0
	s_add_i32 s92, s81, 0
	s_add_i32 s75, s82, 0
	s_add_i32 s76, s75, 0x8000
	s_add_i32 s77, s75, 0x8400
	v_lshlrev_b32_e32 v163, 2, v33
	v_sub_u32_e32 v164, v144, v163
	v_mov_b32_e32 v165, 0
	v_mov_b32_e32 v166, 0xc2800000
	v_bfe_u32 v188, v1, 3, 3
	v_or_b32_e32 v189, s80, v188
	v_lshrrev_b32_e32 v190, 1, v189
	v_bfe_u32 v191, v1, 4, 2
	v_lshrrev_b32_e32 v192, 2, v1
	v_xor_b32_e32 v193, v190, v1
	v_or_b32_e32 v194, s80, v191
	v_xor_b32_e32 v195, v192, v191
	v_lshlrev_b32_e32 v196, 4, v193
	v_lshlrev_b32_e32 v197, 6, v195
	v_lshlrev_b32_e32 v198, 4, v1
	v_lshlrev_b32_e32 v199, 12, v189
	v_and_b32_e32 v200, 0xc0, v197
	v_and_b32_e32 v201, 48, v198
	v_and_or_b32 v152, v196, s1, v199
	v_lshlrev_b32_e32 v202, 12, v194
	v_or3_b32 v153, v201, v200, v202
	v_lshlrev_b32_e32 v203, 2, v1
	v_lshrrev_b32_e32 v204, 1, v1
	v_bfe_u32 v205, v1, 1, 3
	v_bfe_u32 v206, v1, 2, 2
	v_and_b32_e32 v1, 16, v1
	v_and_or_b32 v1, v203, 12, v1
	v_lshl_add_u32 v207, v32, 7, 0
	v_bitop3_b32 v208, v33, v204, 7 bitop3:0x78
	v_and_or_b32 v209, v188, 4, v206
	v_lshl_add_u32 v155, v208, 4, v207
	v_bitop3_b32 v210, v33, v205, 2 bitop3:0x36
	v_lshl_add_u32 v156, v210, 4, v207
	v_bitop3_b32 v211, v33, v205, 4 bitop3:0x36
	v_lshlrev_b32_e32 v212, 8, v209
	v_lshlrev_b32_e32 v1, 1, v1
	v_lshl_add_u32 v157, v211, 4, v207
	v_bitop3_b32 v213, v33, v205, 6 bitop3:0x36
	v_add3_u32 v1, 0, v212, v1
	v_lshlrev_b32_e32 v214, 6, v206
	v_lshl_add_u32 v158, v213, 4, v207
	v_xor_b32_e32 v215, 64, v214
	v_add3_u32 v159, v1, v214, s87
	v_add3_u32 v160, v1, v215, s87
	v_xor_b32_e32 v216, 0x80, v214
	v_xor_b32_e32 v217, 0xc0, v214
	v_add3_u32 v161, v1, v216, s87
	v_add3_u32 v162, v1, v217, s87
	s_mov_b32 m0, s92
	s_nop 0
	global_load_lds_dwordx4 v152, s[64:65]
	v_or_b32_e32 v154, 0x4000, v153
	s_mov_b32 m0, s76
	s_nop 0
	global_load_lds_dwordx4 v153, s[48:49]
	s_mov_b32 m0, s77
	s_nop 0
	global_load_lds_dwordx4 v154, s[48:49]
	s_add_u32 s0, s64, 0x40000
	s_addc_u32 s1, s65, 0
	s_add_i32 s78, s92, 0x2000
	s_mov_b32 m0, s78
	s_nop 0
	global_load_lds_dwordx4 v152, s[0:1]
	s_add_i32 s36, s75, 0xc000
	s_mov_b32 m0, s36
	s_nop 0
	global_load_lds_dwordx4 v153, s[56:57]
	s_add_i32 s37, s75, 0xc400
	s_mov_b32 m0, s37
	s_nop 0
	global_load_lds_dwordx4 v154, s[56:57]
	s_waitcnt vmcnt(9)
	v_and_b32_e32 v19, 0xffff0000, v2
	v_lshlrev_b32_e32 v18, 16, v2
	v_and_b32_e32 v21, 0xffff0000, v3
	v_lshlrev_b32_e32 v20, 16, v3
	v_and_b32_e32 v3, 0xffff0000, v4
	v_lshlrev_b32_e32 v2, 16, v4
	v_and_b32_e32 v23, 0xffff0000, v5
	v_lshlrev_b32_e32 v22, 16, v5
	s_waitcnt vmcnt(8)
	v_and_b32_e32 v5, 0xffff0000, v6
	v_lshlrev_b32_e32 v4, 16, v6
	v_and_b32_e32 v25, 0xffff0000, v7
	v_lshlrev_b32_e32 v24, 16, v7
	v_and_b32_e32 v7, 0xffff0000, v8
	v_lshlrev_b32_e32 v6, 16, v8
	v_and_b32_e32 v27, 0xffff0000, v9
	v_lshlrev_b32_e32 v26, 16, v9
	s_waitcnt vmcnt(7)
	v_and_b32_e32 v9, 0xffff0000, v10
	v_lshlrev_b32_e32 v8, 16, v10
	v_and_b32_e32 v29, 0xffff0000, v11
	v_lshlrev_b32_e32 v28, 16, v11
	v_and_b32_e32 v11, 0xffff0000, v12
	v_lshlrev_b32_e32 v10, 16, v12
	v_and_b32_e32 v31, 0xffff0000, v13
	v_lshlrev_b32_e32 v30, 16, v13
	v_pk_mul_f32 v[12:13], v[18:19], s[44:45] op_sel_hi:[1,0]
	v_pk_mul_f32 v[18:19], v[20:21], s[44:45] op_sel_hi:[1,0]
	v_pk_mul_f32 v[2:3], v[2:3], s[44:45] op_sel_hi:[1,0]
	v_pk_mul_f32 v[20:21], v[22:23], s[44:45] op_sel_hi:[1,0]
	v_pk_mul_f32 v[4:5], v[4:5], s[44:45] op_sel_hi:[1,0]
	v_pk_mul_f32 v[6:7], v[6:7], s[44:45] op_sel_hi:[1,0]
	v_pk_mul_f32 v[22:23], v[24:25], s[44:45] op_sel_hi:[1,0]
	v_pk_mul_f32 v[24:25], v[26:27], s[44:45] op_sel_hi:[1,0]
	v_pk_mul_f32 v[8:9], v[8:9], s[44:45] op_sel_hi:[1,0]
	v_pk_mul_f32 v[26:27], v[28:29], s[44:45] op_sel_hi:[1,0]
	v_pk_mul_f32 v[28:29], v[30:31], s[44:45] op_sel_hi:[1,0]
	v_bfe_u32 v31, v20, 16, 1
	v_bfe_u32 v34, v3, 16, 1
	v_bfe_u32 v38, v13, 16, 1
	v_bfe_u32 v39, v12, 16, 1
	v_bfe_u32 v43, v6, 16, 1
	v_bfe_u32 v46, v5, 16, 1
	v_bfe_u32 v35, v2, 16, 1
	v_add3_u32 v12, v12, v39, s85
	v_add3_u32 v13, v13, v38, s85
	v_add3_u32 v3, v3, v34, s85
	v_add3_u32 v20, v20, v31, s85
	v_add3_u32 v31, v5, v46, s85
	v_add3_u32 v34, v6, v43, s85
	v_bfe_u32 v5, v9, 16, 1
	v_bfe_u32 v6, v8, 16, 1
	v_pk_mul_f32 v[10:11], v[10:11], s[44:45] op_sel_hi:[1,0]
	v_bfe_u32 v30, v21, 16, 1
	v_bfe_u32 v36, v19, 16, 1
	v_bfe_u32 v37, v18, 16, 1
	v_bfe_u32 v47, v4, 16, 1
	v_add3_u32 v2, v2, v35, s85
	v_perm_b32 v128, v13, v12, s86
	v_add3_u32 v12, v8, v6, s85
	v_add3_u32 v13, v9, v5, s85
	s_waitcnt vmcnt(6)
; #define LAS __attribute__((address_space(3)))
; __device__ __forceinline__ bf16 f2bf(float f) { unsigned u = __float_as_uint(f); return (bf16)((u + 0x7fffu + ((u >> 16) & 1u)) >> 16); }
; #define ATT_ISSUE(st_, sl) do { _Pragma("unroll") for (int sb_ = 0; sb_ < NSUB; ++sb_) ATT_DMA(ATT_TILE((st_) * NSUB + sb_), sl, sb_); } while (0)
; #define ATT_WAIT_PREV() do { if (NSUB == 1) { if (nvm == 2) asm volatile("s_waitcnt vmcnt(2)" ::: "memory"); else asm volatile("s_waitcnt vmcnt(3)" ::: "memory"); } \
;                               else { if (nvm == 2) asm volatile("s_waitcnt vmcnt(4)" ::: "memory"); else asm volatile("s_waitcnt vmcnt(6)" ::: "memory"); } } while (0)
; #define ATT_BAR() asm volatile("s_waitcnt lgkmcnt(0)\n\ts_barrier" ::: "memory")
; template <int MODE, int DQK, int DV>
; __device__ __forceinline__ void attn_pass(LAS unsigned char* lds, const Tens& T, size_t rowbase, int q0, f32x16 (&o)[DV / 32], float& l_out, const int wave, QPre* qp = nullptr) {
;     ...
;                 for (int j = 0; j < 8; ++j) a[j] = (short)f2bf(__uint_as_float(((unsigned)(unsigned short)a[j]) << 16) * T.scale2);
;             }
;             qf[s] = a;
;         }
;     ...
;     float m = -64.0f, l = 0.f;
;     bf16x8 kone = {0, 0, 0, 0, 0, 0, 0, 0}, qm = kone;
;     if (MODE == AM_DSA) { if (h == 0) { kone[0] = (short)0x3F80; kone[1] = (short)0x3F80; kone[2] = (short)0x3F80; } qm = split3_bf16(64.0f, h); }
;     f32x16 negm;
; #pragma unroll
;     for (int rg = 0; rg < 16; ++rg) negm[rg] = 64.0f;
; #pragma unroll
;     for (int i = 0; i < NDB; ++i) o[i] = f32x16{};
;     const int jlast = (q0 + wave * 32) / 64;
;     constexpr bool DESC = (MODE == AM_FOX);
;     ...
;     bool wdone = false;
;     volatile LAS int* dflag = (volatile LAS int*)(lds + OFF_MISC + 16);
;     const int nst = ntile / NSUB;
;     ATT_ISSUE(0, 0);
;     if (NRING == 3) ATT_ISSUE(1, 1);
;     if (NRING == 3) ATT_WAIT_PREV(); else asm volatile("s_waitcnt vmcnt(0)" ::: "memory");
;     ATT_BAR();
	v_and_b32_e32 v9, 0xffff0000, v17
	v_lshlrev_b32_e32 v8, 16, v17
	v_bfe_u32 v42, v7, 16, 1
	v_add3_u32 v18, v18, v37, s85
	v_add3_u32 v19, v19, v36, s85
	v_add3_u32 v21, v21, v30, s85
	v_add3_u32 v30, v4, v47, s85
	v_perm_b32 v130, v3, v2, s86
	v_bfe_u32 v2, v10, 16, 1
	v_bfe_u32 v3, v27, 16, 1
	v_bfe_u32 v4, v26, 16, 1
	v_pk_mul_f32 v[8:9], v[8:9], s[44:45] op_sel_hi:[1,0]
	v_add3_u32 v35, v7, v42, s85
	v_perm_b32 v129, v19, v18, s86
	v_add3_u32 v18, v26, v4, s85
	v_add3_u32 v19, v27, v3, s85
	v_add3_u32 v10, v10, v2, s85
	v_and_b32_e32 v3, 0xffff0000, v14
	v_lshlrev_b32_e32 v2, 16, v14
	v_and_b32_e32 v5, 0xffff0000, v15
	v_lshlrev_b32_e32 v4, 16, v15
	v_and_b32_e32 v7, 0xffff0000, v16
	v_lshlrev_b32_e32 v6, 16, v16
	v_bfe_u32 v14, v9, 16, 1
	v_pk_mul_f32 v[4:5], v[4:5], s[44:45] op_sel_hi:[1,0]
	v_pk_mul_f32 v[6:7], v[6:7], s[44:45] op_sel_hi:[1,0]
	v_bfe_u32 v15, v8, 16, 1
	v_add3_u32 v9, v9, v14, s85
	v_bfe_u32 v16, v7, 16, 1
	v_bfe_u32 v17, v6, 16, 1
	v_bfe_u32 v27, v4, 16, 1
	v_add3_u32 v8, v8, v15, s85
	v_bfe_u32 v26, v5, 16, 1
	v_add3_u32 v4, v4, v27, s85
	v_add3_u32 v6, v6, v17, s85
	v_add3_u32 v7, v7, v16, s85
	v_add3_u32 v5, v5, v26, s85
	v_bfe_u32 v48, v29, 16, 1
	v_bfe_u32 v49, v28, 16, 1
	v_pk_mul_f32 v[2:3], v[2:3], s[44:45] op_sel_hi:[1,0]
	v_bfe_u32 v40, v25, 16, 1
	v_bfe_u32 v41, v24, 16, 1
	v_bfe_u32 v44, v23, 16, 1
	v_bfe_u32 v45, v22, 16, 1
	v_bfe_u32 v50, v11, 16, 1
	v_perm_b32 v131, v21, v20, s86
	v_add3_u32 v20, v28, v49, s85
	v_add3_u32 v21, v29, v48, s85
	v_bfe_u32 v28, v3, 16, 1
	v_bfe_u32 v29, v2, 16, 1
	s_waitcnt vmcnt(0)
	v_add3_u32 v22, v22, v45, s85
	v_add3_u32 v23, v23, v44, s85
	v_add3_u32 v24, v24, v41, s85
	v_add3_u32 v25, v25, v40, s85
	v_add3_u32 v11, v11, v50, s85
	v_add3_u32 v2, v2, v29, s85
	v_add3_u32 v3, v3, v28, s85
	s_waitcnt lgkmcnt(0)
	s_barrier
	v_perm_b32 v132, v31, v30, s86
	v_mov_b32_e32 v14, v0
	v_mov_b32_e32 v15, v0
	v_mov_b32_e32 v30, v145
	v_mov_b32_e32 v31, v145
	v_perm_b32 v135, v25, v24, s86
	v_perm_b32 v134, v35, v34, s86
	v_perm_b32 v133, v23, v22, s86
	v_perm_b32 v139, v21, v20, s86
	v_perm_b32 v138, v11, v10, s86
	v_perm_b32 v137, v19, v18, s86
	v_perm_b32 v136, v13, v12, s86
	v_perm_b32 v143, v9, v8, s86
	v_perm_b32 v142, v7, v6, s86
	v_perm_b32 v141, v5, v4, s86
	v_perm_b32 v140, v3, v2, s86
	v_mov_b32_e32 v1, v0
	v_mov_b32_e32 v2, v0
	v_mov_b32_e32 v3, v0
	v_mov_b32_e32 v4, v0
	v_mov_b32_e32 v5, v0
	v_mov_b32_e32 v6, v0
	v_mov_b32_e32 v7, v0
	v_mov_b32_e32 v8, v0
	v_mov_b32_e32 v9, v0
	v_mov_b32_e32 v10, v0
	v_mov_b32_e32 v11, v0
	v_mov_b32_e32 v12, v0
	v_mov_b32_e32 v13, v0
	v_mov_b32_e32 v16, v145
	v_mov_b32_e32 v17, v145
	v_mov_b32_e32 v18, v145
	v_mov_b32_e32 v19, v145
	v_mov_b32_e32 v20, v145
	v_mov_b32_e32 v21, v145
	v_mov_b32_e32 v22, v145
	v_mov_b32_e32 v23, v145
	v_mov_b32_e32 v24, v145
	v_mov_b32_e32 v25, v145
	v_mov_b32_e32 v26, v145
	v_mov_b32_e32 v27, v145
	v_mov_b32_e32 v28, v145
	v_mov_b32_e32 v29, v145
	v_mov_b64_e32 v[78:79], v[30:31]
	v_mov_b64_e32 v[62:63], v[30:31]
	v_mov_b64_e32 v[46:47], v[30:31]
	v_mov_b64_e32 v[94:95], v[14:15]
	s_mov_b32 s0, 0
	v_mov_b64_e32 v[76:77], v[28:29]
	v_mov_b64_e32 v[74:75], v[26:27]
	v_mov_b64_e32 v[72:73], v[24:25]
	v_mov_b64_e32 v[70:71], v[22:23]
	v_mov_b64_e32 v[68:69], v[20:21]
	v_mov_b64_e32 v[66:67], v[18:19]
	v_mov_b64_e32 v[64:65], v[16:17]
	v_mov_b64_e32 v[60:61], v[28:29]
	v_mov_b64_e32 v[58:59], v[26:27]
	v_mov_b64_e32 v[56:57], v[24:25]
	v_mov_b64_e32 v[54:55], v[22:23]
	v_mov_b64_e32 v[52:53], v[20:21]
	v_mov_b64_e32 v[50:51], v[18:19]
	v_mov_b64_e32 v[48:49], v[16:17]
	v_mov_b64_e32 v[44:45], v[28:29]
	v_mov_b64_e32 v[42:43], v[26:27]
	v_mov_b64_e32 v[40:41], v[24:25]
	v_mov_b64_e32 v[38:39], v[22:23]
	v_mov_b64_e32 v[36:37], v[20:21]
	v_mov_b64_e32 v[34:35], v[18:19]
	v_mov_b64_e32 v[32:33], v[16:17]
	v_mov_b64_e32 v[92:93], v[12:13]
	v_mov_b64_e32 v[90:91], v[10:11]
	v_mov_b64_e32 v[88:89], v[8:9]
	v_mov_b64_e32 v[86:87], v[6:7]
	v_mov_b64_e32 v[84:85], v[4:5]
	v_mov_b64_e32 v[82:83], v[2:3]
	v_mov_b64_e32 v[80:81], v[0:1]
	s_branch .LBB0_2441
